# attention softmax VALU: mhat subtraction and row-sum chains as v_pk_add_f32 (steady loop + band subs); MoE-up K-loop first iteration peeled with C=0
# baseline (speedup 1.0000x reference)
.LBB0_688:
	ds_read_b128 v[66:69], v167
	ds_read_b128 v[70:73], v167 offset:32
	ds_read_b128 v[74:77], v167 offset:64
	ds_read_b128 v[78:81], v167 offset:96
	ds_read_b128 v[162:165], v167 offset:128
	ds_read_b128 v[174:177], v167 offset:160
	ds_read_b128 v[178:181], v167 offset:192
	ds_read_b128 v[204:207], v167 offset:224
	v_add_u32_e32 v169, s14, v202
	s_waitcnt lgkmcnt(4)
	v_pk_add_f32 v[96:97], v[80:81], v[200:201] op_sel:[0,1] neg_lo:[0,1] neg_hi:[0,1]
	v_pk_add_f32 v[94:95], v[78:79], v[200:201] op_sel:[0,1] neg_lo:[0,1] neg_hi:[0,1]
	v_pk_add_f32 v[92:93], v[76:77], v[200:201] op_sel:[0,1] neg_lo:[0,1] neg_hi:[0,1]
	v_pk_add_f32 v[90:91], v[74:75], v[200:201] op_sel:[0,1] neg_lo:[0,1] neg_hi:[0,1]
	v_pk_add_f32 v[88:89], v[72:73], v[200:201] op_sel:[0,1] neg_lo:[0,1] neg_hi:[0,1]
	v_pk_add_f32 v[86:87], v[70:71], v[200:201] op_sel:[0,1] neg_lo:[0,1] neg_hi:[0,1]
	v_pk_add_f32 v[84:85], v[68:69], v[200:201] op_sel:[0,1] neg_lo:[0,1] neg_hi:[0,1]
	v_pk_add_f32 v[82:83], v[66:67], v[200:201] op_sel:[0,1] neg_lo:[0,1] neg_hi:[0,1]
	s_waitcnt lgkmcnt(0)
	v_pk_add_f32 v[80:81], v[206:207], v[200:201] op_sel:[0,1] neg_lo:[0,1] neg_hi:[0,1]
	v_pk_add_f32 v[78:79], v[204:205], v[200:201] op_sel:[0,1] neg_lo:[0,1] neg_hi:[0,1]
	v_pk_add_f32 v[76:77], v[180:181], v[200:201] op_sel:[0,1] neg_lo:[0,1] neg_hi:[0,1]
	v_pk_add_f32 v[74:75], v[178:179], v[200:201] op_sel:[0,1] neg_lo:[0,1] neg_hi:[0,1]
	v_pk_add_f32 v[72:73], v[176:177], v[200:201] op_sel:[0,1] neg_lo:[0,1] neg_hi:[0,1]
	v_pk_add_f32 v[70:71], v[174:175], v[200:201] op_sel:[0,1] neg_lo:[0,1] neg_hi:[0,1]
	v_pk_add_f32 v[68:69], v[164:165], v[200:201] op_sel:[0,1] neg_lo:[0,1] neg_hi:[0,1]
	v_pk_add_f32 v[66:67], v[162:163], v[200:201] op_sel:[0,1] neg_lo:[0,1] neg_hi:[0,1]
	ds_read_b64_tr_b16 v[162:163], v169 offset:28672
	ds_read_b64_tr_b16 v[164:165], v169 offset:29184
	v_mfma_f32_32x32x16_bf16 v[82:97], v[158:161], v[114:117], v[82:97]
	v_pk_add_f32 v[110:111], v[50:51], v[52:53]
	v_pk_add_f32 v[110:111], v[110:111], v[54:55]
	v_cvt_pk_bf16_f32 v126, v50, v51
	v_cvt_pk_bf16_f32 v127, v52, v53
	ds_read_b64_tr_b16 v[50:51], v169 offset:32768
	ds_read_b64_tr_b16 v[52:53], v169 offset:33280
	v_mfma_f32_32x32x16_bf16 v[66:81], v[154:157], v[114:117], v[66:81]
	v_pk_add_f32 v[110:111], v[110:111], v[56:57]
	v_pk_add_f32 v[110:111], v[110:111], v[58:59]
	v_cvt_pk_bf16_f32 v128, v54, v55
	v_cvt_pk_bf16_f32 v129, v56, v57
	ds_read_b64_tr_b16 v[54:55], v169 offset:29696
	ds_read_b64_tr_b16 v[56:57], v169 offset:30208
	v_mfma_f32_32x32x16_bf16 v[82:97], v[150:153], v[106:109], v[82:97]
	v_pk_add_f32 v[110:111], v[110:111], v[60:61]
	v_pk_add_f32 v[110:111], v[110:111], v[62:63]
	v_cvt_pk_bf16_f32 v122, v58, v59
	v_cvt_pk_bf16_f32 v123, v60, v61
	ds_read_b64_tr_b16 v[58:59], v169 offset:33792
	ds_read_b64_tr_b16 v[60:61], v169 offset:34304
	v_mfma_f32_32x32x16_bf16 v[66:81], v[146:149], v[106:109], v[66:81]
	v_pk_add_f32 v[110:111], v[110:111], v[64:65]
	v_pk_add_f32 v[110:111], v[110:111], v[34:35]
	v_cvt_pk_bf16_f32 v124, v62, v63
	v_cvt_pk_bf16_f32 v125, v64, v65
	ds_read_b64_tr_b16 v[62:63], v169 offset:30720
	ds_read_b64_tr_b16 v[64:65], v169 offset:31232
	v_mfma_f32_32x32x16_bf16 v[82:97], v[142:145], v[102:105], v[82:97]
	v_pk_add_f32 v[110:111], v[110:111], v[36:37]
	v_pk_add_f32 v[110:111], v[110:111], v[38:39]
	v_cvt_pk_bf16_f32 v118, v34, v35
	v_cvt_pk_bf16_f32 v119, v36, v37
	ds_read_b64_tr_b16 v[34:35], v169 offset:34816
	ds_read_b64_tr_b16 v[36:37], v169 offset:35328
	v_mfma_f32_32x32x16_bf16 v[66:81], v[138:141], v[102:105], v[66:81]
	v_pk_add_f32 v[110:111], v[110:111], v[40:41]
	v_pk_add_f32 v[110:111], v[110:111], v[42:43]
	v_cvt_pk_bf16_f32 v120, v38, v39
	v_cvt_pk_bf16_f32 v121, v40, v41
	ds_read_b64_tr_b16 v[38:39], v169 offset:31744
	ds_read_b64_tr_b16 v[40:41], v169 offset:32256
	v_mfma_f32_32x32x16_bf16 v[82:97], v[134:137], v[98:101], v[82:97]
	v_pk_add_f32 v[110:111], v[110:111], v[44:45]
	v_pk_add_f32 v[134:135], v[110:111], v[46:47]
	v_cvt_pk_bf16_f32 v110, v42, v43
	v_cvt_pk_bf16_f32 v111, v44, v45
	ds_read_b64_tr_b16 v[42:43], v169 offset:35840
	ds_read_b64_tr_b16 v[44:45], v169 offset:36352
	v_mfma_f32_32x32x16_bf16 v[66:81], v[130:133], v[98:101], v[66:81]
	v_pk_add_f32 v[134:135], v[134:135], v[48:49]
	v_add_f32_e32 v130, v134, v135
	v_cvt_pk_bf16_f32 v112, v46, v47
	v_cvt_pk_bf16_f32 v113, v48, v49
	v_lshl_add_u64 v[174:175], v[172:173], 0, s[96:97]
	s_mov_b64 s[14:15], 0x4d280400
	v_lshl_add_u64 v[46:47], v[174:175], 0, s[14:15]
	s_add_i32 s14, s25, s13
	s_mov_b32 s15, m0
	s_mov_b32 m0, s14
	s_nop 0
	global_load_lds_dwordx4 v[46:47], off
	s_mov_b32 m0, s15
	v_lshl_add_u64 v[176:177], v[170:171], 0, s[96:97]
	s_mov_b64 s[14:15], 0x4d140800
	v_lshl_add_u64 v[46:47], v[176:177], 0, s[14:15]
	s_add_i32 s14, s69, s16
	s_mov_b32 s15, m0
	s_mov_b32 m0, s14
	s_nop 0
	global_load_lds_dwordx4 v[46:47], off
	s_mov_b32 m0, s15
	v_max_f32_e32 v46, v83, v83
	v_max_f32_e32 v47, v82, v82
	v_max_f32_e32 v46, v47, v46
	v_max3_f32 v47, v84, v85, v67
	v_max3_f32 v46, v46, v66, v68
	v_max3_f32 v46, v46, v69, v86
	v_max3_f32 v47, v47, v88, v89
	v_max3_f32 v46, v46, v87, v70
	v_max3_f32 v47, v47, v72, v73
	v_max3_f32 v46, v46, v71, v90
	v_max3_f32 v47, v47, v92, v93
	v_max3_f32 v46, v46, v91, v74
	v_max3_f32 v47, v47, v76, v77
	v_max3_f32 v46, v46, v75, v94
	v_max3_f32 v47, v47, v96, v97
	v_max3_f32 v46, v46, v95, v78
	v_max3_f32 v47, v47, v80, v81
	v_max3_f32 v46, v46, v79, v47
	v_mov_b32_e32 v47, v46
	s_nop 1
	v_permlane32_swap_b32_e32 v46, v47
	v_max_f32_e32 v47, v47, v47
	v_max_f32_e32 v46, v46, v46
	v_max_f32_e32 v46, v46, v47
	v_cmp_lt_f32_e32 vcc, s37, v46
	s_cmp_lg_u64 vcc, 0
	v_add_f32_e32 v169, v203, v130
	s_cselect_b64 s[44:45], -1, 0
	s_cbranch_vccnz .LBB0_696

.LBB0_691:
	s_add_i32 s14, s69, 0x2000
	s_cmpk_lg_i32 s69, 0x4000
	s_cselect_b32 s24, s14, 0
	ds_read_b128 v[34:37], v167 offset:256
	ds_read_b128 v[38:41], v167 offset:288
	ds_read_b128 v[42:45], v167 offset:320
	ds_read_b128 v[46:49], v167 offset:352
	ds_read_b128 v[150:153], v167 offset:384
	ds_read_b128 v[178:181], v167 offset:416
	ds_read_b128 v[204:207], v167 offset:448
	ds_read_b128 v[208:211], v167 offset:480
	v_add_u32_e32 v203, s25, v202
	s_waitcnt lgkmcnt(4)
	v_pk_add_f32 v[64:65], v[48:49], v[200:201] op_sel:[0,1] neg_lo:[0,1] neg_hi:[0,1]
	v_pk_add_f32 v[62:63], v[46:47], v[200:201] op_sel:[0,1] neg_lo:[0,1] neg_hi:[0,1]
	v_pk_add_f32 v[60:61], v[44:45], v[200:201] op_sel:[0,1] neg_lo:[0,1] neg_hi:[0,1]
	v_pk_add_f32 v[58:59], v[42:43], v[200:201] op_sel:[0,1] neg_lo:[0,1] neg_hi:[0,1]
	v_pk_add_f32 v[56:57], v[40:41], v[200:201] op_sel:[0,1] neg_lo:[0,1] neg_hi:[0,1]
	v_pk_add_f32 v[54:55], v[38:39], v[200:201] op_sel:[0,1] neg_lo:[0,1] neg_hi:[0,1]
	v_pk_add_f32 v[52:53], v[36:37], v[200:201] op_sel:[0,1] neg_lo:[0,1] neg_hi:[0,1]
	v_pk_add_f32 v[50:51], v[34:35], v[200:201] op_sel:[0,1] neg_lo:[0,1] neg_hi:[0,1]
	s_waitcnt lgkmcnt(0)
	v_pk_add_f32 v[48:49], v[210:211], v[200:201] op_sel:[0,1] neg_lo:[0,1] neg_hi:[0,1]
	v_pk_add_f32 v[46:47], v[208:209], v[200:201] op_sel:[0,1] neg_lo:[0,1] neg_hi:[0,1]
	v_pk_add_f32 v[44:45], v[206:207], v[200:201] op_sel:[0,1] neg_lo:[0,1] neg_hi:[0,1]
	v_pk_add_f32 v[42:43], v[204:205], v[200:201] op_sel:[0,1] neg_lo:[0,1] neg_hi:[0,1]
	v_pk_add_f32 v[40:41], v[180:181], v[200:201] op_sel:[0,1] neg_lo:[0,1] neg_hi:[0,1]
	v_pk_add_f32 v[38:39], v[178:179], v[200:201] op_sel:[0,1] neg_lo:[0,1] neg_hi:[0,1]
	v_pk_add_f32 v[36:37], v[152:153], v[200:201] op_sel:[0,1] neg_lo:[0,1] neg_hi:[0,1]
	v_pk_add_f32 v[34:35], v[150:151], v[200:201] op_sel:[0,1] neg_lo:[0,1] neg_hi:[0,1]
	ds_read_b64_tr_b16 v[150:151], v203 offset:28672
	ds_read_b64_tr_b16 v[152:153], v203 offset:29184
	v_mfma_f32_32x32x16_bf16 v[50:65], v[162:165], v[114:117], v[50:65]
	v_pk_add_f32 v[110:111], v[82:83], v[84:85]
	v_pk_add_f32 v[110:111], v[110:111], v[86:87]
	v_cvt_pk_bf16_f32 v126, v82, v83
	v_cvt_pk_bf16_f32 v127, v84, v85
	ds_read_b64_tr_b16 v[82:83], v203 offset:32768
	ds_read_b64_tr_b16 v[84:85], v203 offset:33280
	v_mfma_f32_32x32x16_bf16 v[34:49], v[158:161], v[114:117], v[34:49]
	v_pk_add_f32 v[110:111], v[110:111], v[88:89]
	v_pk_add_f32 v[110:111], v[110:111], v[90:91]
	v_cvt_pk_bf16_f32 v128, v86, v87
	v_cvt_pk_bf16_f32 v129, v88, v89
	ds_read_b64_tr_b16 v[86:87], v203 offset:29696
	ds_read_b64_tr_b16 v[88:89], v203 offset:30208
	v_mfma_f32_32x32x16_bf16 v[50:65], v[154:157], v[106:109], v[50:65]
	v_pk_add_f32 v[110:111], v[110:111], v[92:93]
	v_pk_add_f32 v[110:111], v[110:111], v[94:95]
	v_cvt_pk_bf16_f32 v122, v90, v91
	v_cvt_pk_bf16_f32 v123, v92, v93
	ds_read_b64_tr_b16 v[90:91], v203 offset:33792
	ds_read_b64_tr_b16 v[92:93], v203 offset:34304
	v_mfma_f32_32x32x16_bf16 v[34:49], v[146:149], v[106:109], v[34:49]
	v_pk_add_f32 v[110:111], v[110:111], v[96:97]
	v_pk_add_f32 v[110:111], v[110:111], v[66:67]
	v_cvt_pk_bf16_f32 v124, v94, v95
	v_cvt_pk_bf16_f32 v125, v96, v97
	ds_read_b64_tr_b16 v[94:95], v203 offset:30720
	ds_read_b64_tr_b16 v[96:97], v203 offset:31232
	v_mfma_f32_32x32x16_bf16 v[50:65], v[142:145], v[102:105], v[50:65]
	v_pk_add_f32 v[110:111], v[110:111], v[68:69]
	v_pk_add_f32 v[110:111], v[110:111], v[70:71]
	v_cvt_pk_bf16_f32 v118, v66, v67
	v_cvt_pk_bf16_f32 v119, v68, v69
	ds_read_b64_tr_b16 v[66:67], v203 offset:34816
	ds_read_b64_tr_b16 v[68:69], v203 offset:35328
	v_mfma_f32_32x32x16_bf16 v[34:49], v[138:141], v[102:105], v[34:49]
	v_pk_add_f32 v[110:111], v[110:111], v[72:73]
	v_pk_add_f32 v[110:111], v[110:111], v[74:75]
	v_cvt_pk_bf16_f32 v120, v70, v71
	v_cvt_pk_bf16_f32 v121, v72, v73
	ds_read_b64_tr_b16 v[70:71], v203 offset:31744
	ds_read_b64_tr_b16 v[72:73], v203 offset:32256
	v_mfma_f32_32x32x16_bf16 v[50:65], v[134:137], v[98:101], v[50:65]
	v_pk_add_f32 v[110:111], v[110:111], v[76:77]
	v_pk_add_f32 v[134:135], v[110:111], v[78:79]
	v_cvt_pk_bf16_f32 v110, v74, v75
	v_cvt_pk_bf16_f32 v111, v76, v77
	ds_read_b64_tr_b16 v[74:75], v203 offset:35840
	ds_read_b64_tr_b16 v[76:77], v203 offset:36352
	v_mfma_f32_32x32x16_bf16 v[34:49], v[130:133], v[98:101], v[34:49]
	v_pk_add_f32 v[134:135], v[134:135], v[80:81]
	v_add_f32_e32 v130, v134, v135
	v_cvt_pk_bf16_f32 v112, v78, v79
	v_cvt_pk_bf16_f32 v113, v80, v81
	s_mov_b64 s[14:15], 0x4d320400
	v_lshl_add_u64 v[78:79], v[174:175], 0, s[14:15]
	s_add_i32 s14, s69, s13
	s_mov_b32 s15, m0
	s_mov_b32 m0, s14
	s_nop 0
	global_load_lds_dwordx4 v[78:79], off
	s_mov_b32 m0, s15
	s_mov_b64 s[14:15], 0x4d1e0800
	v_lshl_add_u64 v[78:79], v[176:177], 0, s[14:15]
	s_add_i32 s14, s24, s16
	s_mov_b32 s15, m0
	s_mov_b32 m0, s14
	s_nop 0
	global_load_lds_dwordx4 v[78:79], off
	s_mov_b32 m0, s15
	v_max_f32_e32 v78, v51, v51
	v_max_f32_e32 v79, v50, v50
	v_max_f32_e32 v78, v79, v78
	v_max3_f32 v79, v52, v53, v35
	v_max3_f32 v78, v78, v34, v36
	v_max3_f32 v78, v78, v37, v54
	v_max3_f32 v79, v79, v56, v57
	v_max3_f32 v78, v78, v55, v38
	v_max3_f32 v79, v79, v40, v41
	v_max3_f32 v78, v78, v39, v58
	v_max3_f32 v79, v79, v60, v61
	v_max3_f32 v78, v78, v59, v42
	v_max3_f32 v79, v79, v44, v45
	v_max3_f32 v78, v78, v43, v62
	v_max3_f32 v79, v79, v64, v65
	v_max3_f32 v78, v78, v63, v46
	v_max3_f32 v79, v79, v48, v49
	v_max3_f32 v78, v78, v47, v79
	v_mov_b32_e32 v79, v78
	s_nop 1
	v_permlane32_swap_b32_e32 v78, v79
	v_max_f32_e32 v79, v79, v79
	v_max_f32_e32 v78, v78, v78
	v_max_f32_e32 v78, v78, v79
	v_cmp_lt_f32_e32 vcc, s37, v78
	s_cmp_lg_u64 vcc, 0
	v_add_f32_e32 v203, v169, v130
	s_cselect_b64 s[44:45], -1, 0
	s_cbranch_vccnz .LBB0_699

.LBB0_712:
	v_lshl_add_u32 v78, s17, 8, v199
	v_add_u32_e32 v66, 0xffffff00, v78
	v_add_u32_e32 v70, 0xffffff80, v78
	ds_read_b128 v[66:69], v66
	ds_read_b128 v[82:85], v70
	v_add_u32_e32 v70, 0xffffff20, v78
	v_add_u32_e32 v74, 0xffffffa0, v78
	ds_read_b128 v[70:73], v70
	ds_read_b128 v[86:89], v74
	v_add_u32_e32 v79, 0xffffff40, v78
	v_subrev_u32_e32 v80, 64, v78
	v_add_u32_e32 v74, 0xffffff60, v78
	v_subrev_u32_e32 v78, 32, v78
	ds_read_b128 v[74:77], v74
	ds_read_b128 v[90:93], v79
	ds_read_b128 v[162:165], v80
	ds_read_b128 v[94:97], v78
	s_waitcnt lgkmcnt(7)
	v_pk_add_f32 v[66:67], v[66:67], v[200:201] op_sel:[0,1] neg_lo:[0,1] neg_hi:[0,1]
	v_add_u32_e32 v166, s51, v202
	s_waitcnt lgkmcnt(3)
	v_pk_add_f32 v[80:81], v[76:77], v[200:201] op_sel:[0,1] neg_lo:[0,1] neg_hi:[0,1]
	v_pk_add_f32 v[78:79], v[74:75], v[200:201] op_sel:[0,1] neg_lo:[0,1] neg_hi:[0,1]
	s_waitcnt lgkmcnt(2)
	v_pk_add_f32 v[76:77], v[92:93], v[200:201] op_sel:[0,1] neg_lo:[0,1] neg_hi:[0,1]
	v_pk_add_f32 v[74:75], v[90:91], v[200:201] op_sel:[0,1] neg_lo:[0,1] neg_hi:[0,1]
	v_pk_add_f32 v[72:73], v[72:73], v[200:201] op_sel:[0,1] neg_lo:[0,1] neg_hi:[0,1]
	v_pk_add_f32 v[70:71], v[70:71], v[200:201] op_sel:[0,1] neg_lo:[0,1] neg_hi:[0,1]
	v_pk_add_f32 v[68:69], v[68:69], v[200:201] op_sel:[0,1] neg_lo:[0,1] neg_hi:[0,1]
	s_waitcnt lgkmcnt(0)
	v_pk_add_f32 v[96:97], v[96:97], v[200:201] op_sel:[0,1] neg_lo:[0,1] neg_hi:[0,1]
	v_pk_add_f32 v[94:95], v[94:95], v[200:201] op_sel:[0,1] neg_lo:[0,1] neg_hi:[0,1]
	v_pk_add_f32 v[92:93], v[164:165], v[200:201] op_sel:[0,1] neg_lo:[0,1] neg_hi:[0,1]
	v_pk_add_f32 v[90:91], v[162:163], v[200:201] op_sel:[0,1] neg_lo:[0,1] neg_hi:[0,1]
	v_pk_add_f32 v[88:89], v[88:89], v[200:201] op_sel:[0,1] neg_lo:[0,1] neg_hi:[0,1]
	v_pk_add_f32 v[86:87], v[86:87], v[200:201] op_sel:[0,1] neg_lo:[0,1] neg_hi:[0,1]
	v_pk_add_f32 v[84:85], v[84:85], v[200:201] op_sel:[0,1] neg_lo:[0,1] neg_hi:[0,1]
	v_pk_add_f32 v[82:83], v[82:83], v[200:201] op_sel:[0,1] neg_lo:[0,1] neg_hi:[0,1]
	ds_read_b64_tr_b16 v[162:163], v166 offset:28672
	ds_read_b64_tr_b16 v[164:165], v166 offset:29184
	v_mfma_f32_32x32x16_bf16 v[66:81], v[158:161], v[114:117], v[66:81]
	v_add_f32_e32 v110, v50, v51
	v_add_f32_e32 v110, v52, v110
	v_add_f32_e32 v110, v53, v110
	v_add_f32_e32 v110, v54, v110
	v_add_f32_e32 v110, v55, v110
	v_cvt_pk_bf16_f32 v126, v50, v51
	v_cvt_pk_bf16_f32 v127, v52, v53
	ds_read_b64_tr_b16 v[158:159], v166 offset:32768
	ds_read_b64_tr_b16 v[160:161], v166 offset:33280
	v_add_f32_e32 v50, v56, v110
	v_add_f32_e32 v50, v57, v50
	v_add_f32_e32 v50, v58, v50
	v_add_f32_e32 v50, v59, v50
	v_cvt_pk_bf16_f32 v128, v54, v55
	v_cvt_pk_bf16_f32 v129, v56, v57
	v_mfma_f32_32x32x16_bf16 v[82:97], v[154:157], v[114:117], v[82:97]
	ds_read_b64_tr_b16 v[114:115], v166 offset:29696
	ds_read_b64_tr_b16 v[116:117], v166 offset:30208
	v_mfma_f32_32x32x16_bf16 v[66:81], v[150:153], v[106:109], v[66:81]
	v_add_f32_e32 v50, v60, v50
	v_add_f32_e32 v50, v61, v50
	v_add_f32_e32 v50, v62, v50
	v_add_f32_e32 v50, v63, v50
	v_cvt_pk_bf16_f32 v122, v58, v59
	v_cvt_pk_bf16_f32 v123, v60, v61
	ds_read_b64_tr_b16 v[150:151], v166 offset:33792
	ds_read_b64_tr_b16 v[152:153], v166 offset:34304
	v_add_f32_e32 v50, v64, v50
	v_add_f32_e32 v50, v65, v50
	v_add_f32_e32 v50, v34, v50
	v_add_f32_e32 v50, v35, v50
	v_cvt_pk_bf16_f32 v124, v62, v63
	v_cvt_pk_bf16_f32 v125, v64, v65
	v_mfma_f32_32x32x16_bf16 v[82:97], v[146:149], v[106:109], v[82:97]
	ds_read_b64_tr_b16 v[106:107], v166 offset:30720
	ds_read_b64_tr_b16 v[108:109], v166 offset:31232
	v_mfma_f32_32x32x16_bf16 v[66:81], v[142:145], v[102:105], v[66:81]
	v_add_f32_e32 v50, v36, v50
	v_add_f32_e32 v50, v37, v50
	v_add_f32_e32 v50, v38, v50
	v_add_f32_e32 v50, v39, v50
	v_cvt_pk_bf16_f32 v118, v34, v35
	v_cvt_pk_bf16_f32 v119, v36, v37
	ds_read_b64_tr_b16 v[142:143], v166 offset:34816
	ds_read_b64_tr_b16 v[144:145], v166 offset:35328
	v_add_f32_e32 v34, v40, v50
	v_add_f32_e32 v34, v41, v34
	v_add_f32_e32 v34, v42, v34
	v_add_f32_e32 v34, v43, v34
	v_cvt_pk_bf16_f32 v120, v38, v39
	v_cvt_pk_bf16_f32 v121, v40, v41
	v_mfma_f32_32x32x16_bf16 v[82:97], v[138:141], v[102:105], v[82:97]
	ds_read_b64_tr_b16 v[102:103], v166 offset:31744
	ds_read_b64_tr_b16 v[104:105], v166 offset:32256
	v_mfma_f32_32x32x16_bf16 v[66:81], v[134:137], v[98:101], v[66:81]
	v_add_f32_e32 v34, v44, v34
	v_add_f32_e32 v34, v45, v34
	v_add_f32_e32 v34, v46, v34
	v_add_f32_e32 v34, v47, v34
	v_cvt_pk_bf16_f32 v110, v42, v43
	v_cvt_pk_bf16_f32 v111, v44, v45
	ds_read_b64_tr_b16 v[134:135], v166 offset:35840
	ds_read_b64_tr_b16 v[136:137], v166 offset:36352
	v_add_f32_e32 v34, v48, v34
	v_add_f32_e32 v34, v49, v34
	v_mfma_f32_32x32x16_bf16 v[82:97], v[130:133], v[98:101], v[82:97]
	v_add_f32_e32 v98, 0, v34
	v_cvt_pk_bf16_f32 v112, v46, v47
	v_cvt_pk_bf16_f32 v113, v48, v49
	v_or_b32_e32 v34, 0xe0, v197
	v_or_b32_e32 v35, 0xc0, v197
	v_cmp_le_i32_e32 vcc, v34, v198
	v_or_b32_e32 v36, 0xc2, v197
	v_or_b32_e32 v37, 0xc3, v197
	s_nop 3
	v_cndmask_b32_e32 v34, v236, v82, vcc
	v_cmp_lt_i32_e32 vcc, v35, v198
	v_or_b32_e32 v38, 0xc8, v197
	v_or_b32_e32 v39, 0xc9, v197
	v_cndmask_b32_e32 v51, v236, v67, vcc
	v_cmp_le_i32_e32 vcc, v35, v198
	v_or_b32_e32 v35, 0xe1, v197
	v_or_b32_e32 v40, 0xca, v197
	v_cndmask_b32_e32 v50, v236, v66, vcc
	v_cmp_le_i32_e32 vcc, v35, v198
	v_or_b32_e32 v41, 0xcb, v197
	v_or_b32_e32 v42, 0xd0, v197
	v_cndmask_b32_e32 v35, v236, v83, vcc
	v_cmp_le_i32_e32 vcc, v36, v198
	v_or_b32_e32 v36, 0xe2, v197
	v_or_b32_e32 v43, 0xd1, v197
	v_cndmask_b32_e32 v52, v236, v68, vcc
	v_cmp_le_i32_e32 vcc, v36, v198
	v_or_b32_e32 v44, 0xd2, v197
	v_or_b32_e32 v45, 0xd3, v197
	v_cndmask_b32_e32 v36, v236, v84, vcc
	v_cmp_le_i32_e32 vcc, v37, v198
	v_or_b32_e32 v37, 0xe3, v197
	v_or_b32_e32 v46, 0xd8, v197
	v_cndmask_b32_e32 v53, v236, v69, vcc
	v_cmp_le_i32_e32 vcc, v37, v198
	v_or_b32_e32 v47, 0xd9, v197
	v_max_f32_e32 v66, v51, v51
	v_cndmask_b32_e32 v37, v236, v85, vcc
	v_cmp_le_i32_e32 vcc, v38, v198
	v_or_b32_e32 v38, 0xe8, v197
	v_max_f32_e32 v67, v50, v50
	v_cndmask_b32_e32 v54, v236, v70, vcc
	v_cmp_le_i32_e32 vcc, v38, v198
	v_max_f32_e32 v66, v67, v66
	v_or_b32_e32 v48, 0xda, v197
	v_cndmask_b32_e32 v38, v236, v86, vcc
	v_cmp_le_i32_e32 vcc, v39, v198
	v_or_b32_e32 v39, 0xe9, v197
	v_max3_f32 v67, v52, v53, v35
	v_cndmask_b32_e32 v55, v236, v71, vcc
	v_cmp_le_i32_e32 vcc, v39, v198
	v_max3_f32 v66, v66, v34, v36
	v_max3_f32 v66, v66, v37, v54
	v_cndmask_b32_e32 v39, v236, v87, vcc
	v_cmp_le_i32_e32 vcc, v40, v198
	v_or_b32_e32 v40, 0xea, v197
	v_or_b32_e32 v49, 0xdb, v197
	v_cndmask_b32_e32 v56, v236, v72, vcc
	v_cmp_le_i32_e32 vcc, v40, v198
	v_max3_f32 v66, v66, v55, v38
	s_nop 0
	v_cndmask_b32_e32 v40, v236, v88, vcc
	v_cmp_le_i32_e32 vcc, v41, v198
	v_or_b32_e32 v41, 0xeb, v197
	s_nop 0
	v_cndmask_b32_e32 v57, v236, v73, vcc
	v_cmp_le_i32_e32 vcc, v41, v198
	v_max3_f32 v67, v67, v56, v57
	s_nop 0
	v_cndmask_b32_e32 v41, v236, v89, vcc
	v_cmp_le_i32_e32 vcc, v42, v198
	v_or_b32_e32 v42, 0xf0, v197
	v_max3_f32 v67, v67, v40, v41
	v_cndmask_b32_e32 v58, v236, v74, vcc
	v_cmp_le_i32_e32 vcc, v42, v198
	v_max3_f32 v66, v66, v39, v58
	s_nop 0
	v_cndmask_b32_e32 v42, v236, v90, vcc
	v_cmp_le_i32_e32 vcc, v43, v198
	v_or_b32_e32 v43, 0xf1, v197
	s_nop 0
	v_cndmask_b32_e32 v59, v236, v75, vcc
	v_cmp_le_i32_e32 vcc, v43, v198
	v_max3_f32 v66, v66, v59, v42
	s_nop 0
	v_cndmask_b32_e32 v43, v236, v91, vcc
	v_cmp_le_i32_e32 vcc, v44, v198
	v_or_b32_e32 v44, 0xf2, v197
	s_nop 0
	v_cndmask_b32_e32 v60, v236, v76, vcc
	v_cmp_le_i32_e32 vcc, v44, v198
	s_nop 1
	v_cndmask_b32_e32 v44, v236, v92, vcc
	v_cmp_le_i32_e32 vcc, v45, v198
	v_or_b32_e32 v45, 0xf3, v197
	s_nop 0
	v_cndmask_b32_e32 v61, v236, v77, vcc
	v_cmp_le_i32_e32 vcc, v45, v198
	v_max3_f32 v67, v67, v60, v61
	s_nop 0
	v_cndmask_b32_e32 v45, v236, v93, vcc
	v_cmp_le_i32_e32 vcc, v46, v198
	v_or_b32_e32 v46, 0xf8, v197
	v_max3_f32 v67, v67, v44, v45
	v_cndmask_b32_e32 v62, v236, v78, vcc
	v_cmp_le_i32_e32 vcc, v46, v198
	v_max3_f32 v66, v66, v43, v62
	s_nop 0
	v_cndmask_b32_e32 v46, v236, v94, vcc
	v_cmp_le_i32_e32 vcc, v47, v198
	v_or_b32_e32 v47, 0xf9, v197
	s_nop 0
	v_cndmask_b32_e32 v63, v236, v79, vcc
	v_cmp_le_i32_e32 vcc, v47, v198
	v_max3_f32 v68, v66, v63, v46
	v_add_f32_e32 v66, v203, v98
	v_cndmask_b32_e32 v47, v236, v95, vcc
	v_cmp_le_i32_e32 vcc, v48, v198
	v_or_b32_e32 v48, 0xfa, v197
	s_nop 0
	v_cndmask_b32_e32 v64, v236, v80, vcc
	v_cmp_le_i32_e32 vcc, v48, v198
	s_nop 1
	v_cndmask_b32_e32 v48, v236, v96, vcc
	v_cmp_le_i32_e32 vcc, v49, v198
	v_or_b32_e32 v49, 0xfb, v197
	s_nop 0
	v_cndmask_b32_e32 v65, v236, v81, vcc
	v_cmp_le_i32_e32 vcc, v49, v198
	v_max3_f32 v67, v67, v64, v65
	s_nop 0
	v_cndmask_b32_e32 v49, v236, v97, vcc
	v_max3_f32 v67, v67, v48, v49
	v_max3_f32 v67, v68, v47, v67
	v_mov_b32_e32 v68, v67
	s_nop 1
	v_permlane32_swap_b32_e32 v67, v68
	v_max_f32_e32 v68, v68, v68
	v_max_f32_e32 v67, v67, v67
	v_max_f32_e32 v67, v67, v68
	v_cmp_lt_f32_e32 vcc, s37, v67
	s_cmp_lg_u64 vcc, 0
	s_cselect_b64 s[0:1], -1, 0
	s_cbranch_vccnz .LBB0_767

.LBB0_719:
	ds_read_b128 v[66:69], v205
	ds_read_b128 v[70:73], v205 offset:32
	ds_read_b128 v[74:77], v205 offset:64
	ds_read_b128 v[78:81], v205 offset:96
	ds_read_b128 v[162:165], v205 offset:128
	ds_read_b128 v[166:169], v205 offset:160
	ds_read_b128 v[170:173], v205 offset:192
	ds_read_b128 v[178:181], v205 offset:224
	s_waitcnt lgkmcnt(4)
	v_pk_add_f32 v[96:97], v[80:81], v[200:201] op_sel:[0,1] neg_lo:[0,1] neg_hi:[0,1]
	v_pk_add_f32 v[94:95], v[78:79], v[200:201] op_sel:[0,1] neg_lo:[0,1] neg_hi:[0,1]
	v_pk_add_f32 v[92:93], v[76:77], v[200:201] op_sel:[0,1] neg_lo:[0,1] neg_hi:[0,1]
	v_pk_add_f32 v[90:91], v[74:75], v[200:201] op_sel:[0,1] neg_lo:[0,1] neg_hi:[0,1]
	v_pk_add_f32 v[88:89], v[72:73], v[200:201] op_sel:[0,1] neg_lo:[0,1] neg_hi:[0,1]
	v_pk_add_f32 v[86:87], v[70:71], v[200:201] op_sel:[0,1] neg_lo:[0,1] neg_hi:[0,1]
	v_pk_add_f32 v[84:85], v[68:69], v[200:201] op_sel:[0,1] neg_lo:[0,1] neg_hi:[0,1]
	v_pk_add_f32 v[82:83], v[66:67], v[200:201] op_sel:[0,1] neg_lo:[0,1] neg_hi:[0,1]
	s_waitcnt lgkmcnt(0)
	v_pk_add_f32 v[80:81], v[180:181], v[200:201] op_sel:[0,1] neg_lo:[0,1] neg_hi:[0,1]
	v_pk_add_f32 v[78:79], v[178:179], v[200:201] op_sel:[0,1] neg_lo:[0,1] neg_hi:[0,1]
	v_pk_add_f32 v[76:77], v[172:173], v[200:201] op_sel:[0,1] neg_lo:[0,1] neg_hi:[0,1]
	v_pk_add_f32 v[74:75], v[170:171], v[200:201] op_sel:[0,1] neg_lo:[0,1] neg_hi:[0,1]
	v_pk_add_f32 v[72:73], v[168:169], v[200:201] op_sel:[0,1] neg_lo:[0,1] neg_hi:[0,1]
	v_pk_add_f32 v[70:71], v[166:167], v[200:201] op_sel:[0,1] neg_lo:[0,1] neg_hi:[0,1]
	v_pk_add_f32 v[68:69], v[164:165], v[200:201] op_sel:[0,1] neg_lo:[0,1] neg_hi:[0,1]
	v_pk_add_f32 v[66:67], v[162:163], v[200:201] op_sel:[0,1] neg_lo:[0,1] neg_hi:[0,1]
	v_add_u32_e32 v186, s69, v202
	ds_read_b64_tr_b16 v[162:163], v186 offset:28672
	ds_read_b64_tr_b16 v[164:165], v186 offset:29184
	v_mfma_f32_32x32x16_bf16 v[82:97], v[158:161], v[114:117], v[82:97]
	v_add_f32_e32 v110, v50, v51
	v_add_f32_e32 v110, v52, v110
	v_add_f32_e32 v110, v53, v110
	v_add_f32_e32 v110, v54, v110
	v_add_f32_e32 v110, v55, v110
	v_cvt_pk_bf16_f32 v126, v50, v51
	v_cvt_pk_bf16_f32 v127, v52, v53
	ds_read_b64_tr_b16 v[50:51], v186 offset:32768
	ds_read_b64_tr_b16 v[52:53], v186 offset:33280
	v_mfma_f32_32x32x16_bf16 v[66:81], v[154:157], v[114:117], v[66:81]
	v_add_f32_e32 v110, v56, v110
	v_add_f32_e32 v110, v57, v110
	v_add_f32_e32 v110, v58, v110
	v_add_f32_e32 v110, v59, v110
	v_cvt_pk_bf16_f32 v128, v54, v55
	v_cvt_pk_bf16_f32 v129, v56, v57
	ds_read_b64_tr_b16 v[54:55], v186 offset:29696
	ds_read_b64_tr_b16 v[56:57], v186 offset:30208
	v_mfma_f32_32x32x16_bf16 v[82:97], v[150:153], v[106:109], v[82:97]
	v_add_f32_e32 v110, v60, v110
	v_add_f32_e32 v110, v61, v110
	v_add_f32_e32 v110, v62, v110
	v_add_f32_e32 v110, v63, v110
	v_cvt_pk_bf16_f32 v122, v58, v59
	v_cvt_pk_bf16_f32 v123, v60, v61
	ds_read_b64_tr_b16 v[58:59], v186 offset:33792
	ds_read_b64_tr_b16 v[60:61], v186 offset:34304
	v_mfma_f32_32x32x16_bf16 v[66:81], v[146:149], v[106:109], v[66:81]
	v_add_f32_e32 v110, v64, v110
	v_add_f32_e32 v110, v65, v110
	v_add_f32_e32 v110, v34, v110
	v_add_f32_e32 v110, v35, v110
	v_cvt_pk_bf16_f32 v124, v62, v63
	v_cvt_pk_bf16_f32 v125, v64, v65
	ds_read_b64_tr_b16 v[62:63], v186 offset:30720
	ds_read_b64_tr_b16 v[64:65], v186 offset:31232
	v_mfma_f32_32x32x16_bf16 v[82:97], v[142:145], v[102:105], v[82:97]
	v_add_f32_e32 v110, v36, v110
	v_add_f32_e32 v110, v37, v110
	v_add_f32_e32 v110, v38, v110
	v_add_f32_e32 v110, v39, v110
	v_cvt_pk_bf16_f32 v118, v34, v35
	v_cvt_pk_bf16_f32 v119, v36, v37
	ds_read_b64_tr_b16 v[34:35], v186 offset:34816
	ds_read_b64_tr_b16 v[36:37], v186 offset:35328
	v_mfma_f32_32x32x16_bf16 v[66:81], v[138:141], v[102:105], v[66:81]
	v_add_f32_e32 v110, v40, v110
	v_add_f32_e32 v110, v41, v110
	v_add_f32_e32 v110, v42, v110
	v_add_f32_e32 v110, v43, v110
	v_cvt_pk_bf16_f32 v120, v38, v39
	v_cvt_pk_bf16_f32 v121, v40, v41
	ds_read_b64_tr_b16 v[38:39], v186 offset:31744
	ds_read_b64_tr_b16 v[40:41], v186 offset:32256
	v_mfma_f32_32x32x16_bf16 v[82:97], v[134:137], v[98:101], v[82:97]
	v_add_f32_e32 v110, v44, v110
	v_add_f32_e32 v110, v45, v110
	v_add_f32_e32 v110, v46, v110
	v_add_f32_e32 v134, v47, v110
	v_cvt_pk_bf16_f32 v110, v42, v43
	v_cvt_pk_bf16_f32 v111, v44, v45
	ds_read_b64_tr_b16 v[42:43], v186 offset:35840
	ds_read_b64_tr_b16 v[44:45], v186 offset:36352
	v_mfma_f32_32x32x16_bf16 v[66:81], v[130:133], v[98:101], v[66:81]
	v_add_f32_e32 v112, v48, v134
	v_add_f32_e32 v112, v49, v112
	v_add_f32_e32 v130, 0, v112
	v_cvt_pk_bf16_f32 v112, v46, v47
	v_cvt_pk_bf16_f32 v113, v48, v49
	s_add_i32 s0, s2, 1
	s_cmp_ge_i32 s0, s17
	s_cselect_b64 s[0:1], -1, 0
	s_and_b64 vcc, exec, s[0:1]
	v_lshl_add_u64 v[180:181], v[176:177], 0, s[96:97]
	s_cbranch_vccnz .LBB0_721
	s_mov_b64 s[14:15], 0x4d1e0400
	v_lshl_add_u64 v[46:47], v[180:181], 0, s[14:15]
	s_add_i32 s14, s24, s13
	s_mov_b32 s15, m0
	s_mov_b32 m0, s14
	s_nop 0
	global_load_lds_dwordx4 v[46:47], off
	s_mov_b32 m0, s15

.LBB0_732:
	ds_read_b128 v[34:37], v205 offset:256
	ds_read_b128 v[38:41], v205 offset:288
	ds_read_b128 v[42:45], v205 offset:320
	ds_read_b128 v[46:49], v205 offset:352
	ds_read_b128 v[162:165], v205 offset:384
	ds_read_b128 v[166:169], v205 offset:416
	ds_read_b128 v[170:173], v205 offset:448
	ds_read_b128 v[206:209], v205 offset:480
	s_waitcnt lgkmcnt(4)
	v_pk_add_f32 v[64:65], v[48:49], v[200:201] op_sel:[0,1] neg_lo:[0,1] neg_hi:[0,1]
	v_pk_add_f32 v[62:63], v[46:47], v[200:201] op_sel:[0,1] neg_lo:[0,1] neg_hi:[0,1]
	v_pk_add_f32 v[60:61], v[44:45], v[200:201] op_sel:[0,1] neg_lo:[0,1] neg_hi:[0,1]
	v_pk_add_f32 v[58:59], v[42:43], v[200:201] op_sel:[0,1] neg_lo:[0,1] neg_hi:[0,1]
	v_pk_add_f32 v[56:57], v[40:41], v[200:201] op_sel:[0,1] neg_lo:[0,1] neg_hi:[0,1]
	v_pk_add_f32 v[54:55], v[38:39], v[200:201] op_sel:[0,1] neg_lo:[0,1] neg_hi:[0,1]
	v_pk_add_f32 v[52:53], v[36:37], v[200:201] op_sel:[0,1] neg_lo:[0,1] neg_hi:[0,1]
	v_pk_add_f32 v[50:51], v[34:35], v[200:201] op_sel:[0,1] neg_lo:[0,1] neg_hi:[0,1]
	s_waitcnt lgkmcnt(0)
	v_pk_add_f32 v[48:49], v[208:209], v[200:201] op_sel:[0,1] neg_lo:[0,1] neg_hi:[0,1]
	v_pk_add_f32 v[46:47], v[206:207], v[200:201] op_sel:[0,1] neg_lo:[0,1] neg_hi:[0,1]
	v_pk_add_f32 v[44:45], v[172:173], v[200:201] op_sel:[0,1] neg_lo:[0,1] neg_hi:[0,1]
	v_pk_add_f32 v[42:43], v[170:171], v[200:201] op_sel:[0,1] neg_lo:[0,1] neg_hi:[0,1]
	v_pk_add_f32 v[40:41], v[168:169], v[200:201] op_sel:[0,1] neg_lo:[0,1] neg_hi:[0,1]
	v_pk_add_f32 v[38:39], v[166:167], v[200:201] op_sel:[0,1] neg_lo:[0,1] neg_hi:[0,1]
	v_pk_add_f32 v[36:37], v[164:165], v[200:201] op_sel:[0,1] neg_lo:[0,1] neg_hi:[0,1]
	v_pk_add_f32 v[34:35], v[162:163], v[200:201] op_sel:[0,1] neg_lo:[0,1] neg_hi:[0,1]
	v_add_u32_e32 v203, s24, v202
	ds_read_b64_tr_b16 v[170:171], v203 offset:28672
	ds_read_b64_tr_b16 v[172:173], v203 offset:29184
	v_mfma_f32_32x32x16_bf16 v[50:65], v[158:161], v[114:117], v[50:65]
	v_add_f32_e32 v110, v82, v83
	v_add_f32_e32 v110, v84, v110
	v_add_f32_e32 v110, v85, v110
	v_add_f32_e32 v110, v86, v110
	v_add_f32_e32 v110, v87, v110
	v_cvt_pk_bf16_f32 v126, v82, v83
	v_cvt_pk_bf16_f32 v127, v84, v85
	ds_read_b64_tr_b16 v[166:167], v203 offset:32768
	ds_read_b64_tr_b16 v[168:169], v203 offset:33280
	v_mfma_f32_32x32x16_bf16 v[34:49], v[154:157], v[114:117], v[34:49]
	v_add_f32_e32 v82, v88, v110
	v_add_f32_e32 v82, v89, v82
	v_add_f32_e32 v82, v90, v82
	v_add_f32_e32 v82, v91, v82
	v_cvt_pk_bf16_f32 v128, v86, v87
	v_cvt_pk_bf16_f32 v129, v88, v89
	ds_read_b64_tr_b16 v[162:163], v203 offset:29696
	ds_read_b64_tr_b16 v[164:165], v203 offset:30208
	v_mfma_f32_32x32x16_bf16 v[50:65], v[150:153], v[106:109], v[50:65]
	v_add_f32_e32 v82, v92, v82
	v_add_f32_e32 v82, v93, v82
	v_add_f32_e32 v82, v94, v82
	v_add_f32_e32 v82, v95, v82
	v_cvt_pk_bf16_f32 v122, v90, v91
	v_cvt_pk_bf16_f32 v123, v92, v93
	ds_read_b64_tr_b16 v[90:91], v203 offset:33792
	ds_read_b64_tr_b16 v[92:93], v203 offset:34304
	v_mfma_f32_32x32x16_bf16 v[34:49], v[146:149], v[106:109], v[34:49]
	v_add_f32_e32 v82, v96, v82
	v_add_f32_e32 v82, v97, v82
	v_add_f32_e32 v82, v66, v82
	v_add_f32_e32 v82, v67, v82
	v_cvt_pk_bf16_f32 v124, v94, v95
	v_cvt_pk_bf16_f32 v125, v96, v97
	ds_read_b64_tr_b16 v[86:87], v203 offset:30720
	ds_read_b64_tr_b16 v[88:89], v203 offset:31232
	v_mfma_f32_32x32x16_bf16 v[50:65], v[142:145], v[102:105], v[50:65]
	v_add_f32_e32 v82, v68, v82
	v_add_f32_e32 v82, v69, v82
	v_add_f32_e32 v82, v70, v82
	v_add_f32_e32 v94, v71, v82
	v_cvt_pk_bf16_f32 v118, v66, v67
	v_cvt_pk_bf16_f32 v119, v68, v69
	ds_read_b64_tr_b16 v[82:83], v203 offset:34816
	ds_read_b64_tr_b16 v[84:85], v203 offset:35328
	v_mfma_f32_32x32x16_bf16 v[34:49], v[138:141], v[102:105], v[34:49]
	v_add_f32_e32 v66, v72, v94
	v_add_f32_e32 v66, v73, v66
	v_add_f32_e32 v66, v74, v66
	v_add_f32_e32 v66, v75, v66
	v_cvt_pk_bf16_f32 v120, v70, v71
	v_cvt_pk_bf16_f32 v121, v72, v73
	ds_read_b64_tr_b16 v[70:71], v203 offset:31744
	ds_read_b64_tr_b16 v[72:73], v203 offset:32256
	v_mfma_f32_32x32x16_bf16 v[50:65], v[134:137], v[98:101], v[50:65]
	v_add_f32_e32 v66, v76, v66
	v_add_f32_e32 v66, v77, v66
	v_add_f32_e32 v66, v78, v66
	v_add_f32_e32 v94, v79, v66
	v_cvt_pk_bf16_f32 v110, v74, v75
	v_cvt_pk_bf16_f32 v111, v76, v77
	ds_read_b64_tr_b16 v[66:67], v203 offset:35840
	ds_read_b64_tr_b16 v[68:69], v203 offset:36352
	v_mfma_f32_32x32x16_bf16 v[34:49], v[130:133], v[98:101], v[34:49]
	v_add_f32_e32 v74, v80, v94
	v_add_f32_e32 v74, v81, v74
	v_add_f32_e32 v74, 0, v74
	v_cvt_pk_bf16_f32 v112, v78, v79
	v_cvt_pk_bf16_f32 v113, v80, v81
	s_add_i32 s35, s2, 2
	s_cmp_ge_i32 s35, s17
	s_cselect_b64 s[44:45], -1, 0
	s_and_b64 vcc, exec, s[44:45]
	s_cbranch_vccnz .LBB0_734
	s_mov_b64 s[14:15], 0x4d280400
	v_lshl_add_u64 v[76:77], v[180:181], 0, s[14:15]
	s_add_i32 s14, s51, s13
	s_mov_b32 s15, m0
	s_mov_b32 m0, s14
	s_nop 0
	global_load_lds_dwordx4 v[76:77], off
	s_mov_b32 m0, s15
